# baseline (speedup 1.0000x reference)
.LBB2_10:
	s_barrier
	s_waitcnt lgkmcnt(0)
	s_add_i32 s17, s17, 4
	s_waitcnt lgkmcnt(0)
	v_mfma_f32_16x16x32_f16 v[2:5], v[114:117], v[106:109], v[2:5]
	v_mfma_f32_16x16x32_f16 v[46:49], v[118:121], v[110:113], v[2:5]
	v_mfma_f32_16x16x32_f16 v[2:5], v[122:125], v[106:109], v[6:9]
	v_mfma_f32_16x16x32_f16 v[38:41], v[126:129], v[110:113], v[2:5]
	v_mfma_f32_16x16x32_f16 v[2:5], v[114:117], v[98:101], v[10:13]
	v_mfma_f32_16x16x32_f16 v[42:45], v[118:121], v[102:105], v[2:5]
	v_mfma_f32_16x16x32_f16 v[2:5], v[122:125], v[98:101], v[14:17]
	v_mfma_f32_16x16x32_f16 v[34:37], v[126:129], v[102:105], v[2:5]
	v_mfma_f32_16x16x32_f16 v[2:5], v[114:117], v[90:93], v[66:69]
	v_mfma_f32_16x16x32_f16 v[14:17], v[118:121], v[94:97], v[2:5]
	v_mfma_f32_16x16x32_f16 v[2:5], v[122:125], v[90:93], v[70:73]
	v_mfma_f32_16x16x32_f16 v[6:9], v[126:129], v[94:97], v[2:5]
	v_mfma_f32_16x16x32_f16 v[2:5], v[114:117], v[82:85], v[74:77]
	v_mfma_f32_16x16x32_f16 v[10:13], v[118:121], v[86:89], v[2:5]
	v_mfma_f32_16x16x32_f16 v[2:5], v[122:125], v[82:85], v[78:81]
	v_mfma_f32_16x16x32_f16 v[2:5], v[126:129], v[86:89], v[2:5]
	s_barrier
	s_add_u32 s24, s24, 0x200
	s_addc_u32 s25, s25, 0
	s_and_b64 vcc, exec, s[26:27]
	s_cbranch_vccnz .LBB2_29
.LBB2_11:
	ds_read_b128 v[66:69], v146
	ds_read_b128 v[70:73], v146 offset:1024
	ds_read_b128 v[74:77], v146 offset:2048
	ds_read_b128 v[78:81], v146 offset:3072
	s_add_u32 s41, s20, s24
	s_addc_u32 s42, s21, s25
	s_add_u32 s26, s41, 0x100
	s_addc_u32 s27, s42, 0
	v_readfirstlane_b32 s28, v151
	v_lshl_add_u64 v[114:115], s[26:27], 0, v[130:131]
	s_mov_b32 m0, s28
	s_add_u32 s39, s22, s24
	ds_read_b128 v[82:85], v147
	ds_read_b128 v[86:89], v147 offset:1024
	ds_read_b128 v[90:93], v148
	ds_read_b128 v[94:97], v148 offset:1024
	ds_read_b128 v[98:101], v149
	ds_read_b128 v[102:105], v149 offset:1024
	ds_read_b128 v[106:109], v150
	ds_read_b128 v[110:113], v150 offset:1024
	global_load_lds_dwordx4 v[114:115], off
	v_lshl_add_u64 v[114:115], s[26:27], 0, v[132:133]
	v_readfirstlane_b32 s26, v152
	s_addc_u32 s40, s23, s25
	s_mov_b32 m0, s26
	s_add_u32 s26, s39, 0x80
	global_load_lds_dwordx4 v[114:115], off
	s_addc_u32 s27, s40, 0
	v_readfirstlane_b32 s28, v153
	s_waitcnt vmcnt(4)
	v_lshl_add_u64 v[114:115], s[26:27], 0, v[130:131]
	s_mov_b32 m0, s28
	s_waitcnt lgkmcnt(8)
	s_barrier
	global_load_lds_dwordx4 v[114:115], off
	v_lshl_add_u64 v[114:115], s[26:27], 0, v[132:133]
	v_readfirstlane_b32 s26, v154
	s_mov_b32 m0, s26
	s_nop 0
	global_load_lds_dwordx4 v[114:115], off
	s_waitcnt lgkmcnt(0)
	s_waitcnt lgkmcnt(0)
	v_mfma_f32_16x16x32_f16 v[22:25], v[74:77], v[98:101], v[22:25]
	v_mfma_f32_16x16x32_f16 v[62:65], v[66:69], v[82:85], v[62:65]
	v_mfma_f32_16x16x32_f16 v[54:57], v[74:77], v[82:85], v[54:57]
	v_mfma_f32_16x16x32_f16 v[58:61], v[66:69], v[90:93], v[58:61]
	v_mfma_f32_16x16x32_f16 v[50:53], v[74:77], v[90:93], v[50:53]
	v_mfma_f32_16x16x32_f16 v[30:33], v[66:69], v[98:101], v[30:33]
	v_mfma_f32_16x16x32_f16 v[118:121], v[78:81], v[102:105], v[22:25]
	v_mfma_f32_16x16x32_f16 v[22:25], v[66:69], v[106:109], v[26:29]
	v_mfma_f32_16x16x32_f16 v[18:21], v[74:77], v[106:109], v[18:21]
	v_mfma_f32_16x16x32_f16 v[62:65], v[70:73], v[86:89], v[62:65]
	v_mfma_f32_16x16x32_f16 v[54:57], v[78:81], v[86:89], v[54:57]
	v_mfma_f32_16x16x32_f16 v[58:61], v[70:73], v[94:97], v[58:61]
	v_mfma_f32_16x16x32_f16 v[50:53], v[78:81], v[94:97], v[50:53]
	v_mfma_f32_16x16x32_f16 v[114:117], v[70:73], v[102:105], v[30:33]
	v_mfma_f32_16x16x32_f16 v[66:69], v[70:73], v[110:113], v[22:25]
	v_mfma_f32_16x16x32_f16 v[70:73], v[78:81], v[110:113], v[18:21]
	s_barrier
	s_add_u32 s37, s18, s24
	s_addc_u32 s38, s19, s25
	s_add_u32 s26, s37, 0x100
	s_addc_u32 s27, s38, 0
	v_readfirstlane_b32 s28, v134
	v_lshl_add_u64 v[74:75], s[26:27], 0, v[130:131]
	s_mov_b32 m0, s28
	ds_read_b128 v[18:21], v155
	ds_read_b128 v[22:25], v155 offset:1024
	ds_read_b128 v[26:29], v155 offset:2048
	ds_read_b128 v[30:33], v155 offset:3072
	global_load_lds_dwordx4 v[74:75], off
	v_lshl_add_u64 v[74:75], s[26:27], 0, v[132:133]
	v_readfirstlane_b32 s26, v135
	s_mov_b32 m0, s26
	s_nop 0
	global_load_lds_dwordx4 v[74:75], off
	s_waitcnt vmcnt(6)
	s_barrier
	s_waitcnt lgkmcnt(0)
	s_waitcnt lgkmcnt(0)
	v_mfma_f32_16x16x32_f16 v[38:41], v[26:29], v[82:85], v[38:41]
	v_mfma_f32_16x16x32_f16 v[46:49], v[18:21], v[82:85], v[46:49]
	v_mfma_f32_16x16x32_f16 v[78:81], v[30:33], v[86:89], v[38:41]
	v_mfma_f32_16x16x32_f16 v[38:41], v[18:21], v[90:93], v[42:45]
	v_mfma_f32_16x16x32_f16 v[34:37], v[26:29], v[90:93], v[34:37]
	v_mfma_f32_16x16x32_f16 v[6:9], v[26:29], v[98:101], v[6:9]
	v_mfma_f32_16x16x32_f16 v[74:77], v[22:25], v[86:89], v[46:49]
	v_mfma_f32_16x16x32_f16 v[82:85], v[22:25], v[94:97], v[38:41]
	v_mfma_f32_16x16x32_f16 v[86:89], v[30:33], v[94:97], v[34:37]
	v_mfma_f32_16x16x32_f16 v[14:17], v[18:21], v[98:101], v[14:17]
	v_mfma_f32_16x16x32_f16 v[94:97], v[30:33], v[102:105], v[6:9]
	v_mfma_f32_16x16x32_f16 v[6:9], v[18:21], v[106:109], v[10:13]
	v_mfma_f32_16x16x32_f16 v[2:5], v[26:29], v[106:109], v[2:5]
	v_mfma_f32_16x16x32_f16 v[90:93], v[22:25], v[102:105], v[14:17]
	v_mfma_f32_16x16x32_f16 v[98:101], v[22:25], v[110:113], v[6:9]
	v_mfma_f32_16x16x32_f16 v[102:105], v[30:33], v[110:113], v[2:5]
	s_barrier
	s_nop 2
	ds_read_b128 v[2:5], v156
	ds_read_b128 v[6:9], v156 offset:1024
	ds_read_b128 v[10:13], v156 offset:2048
	ds_read_b128 v[14:17], v156 offset:3072
	s_add_u32 s26, s41, 0x180
	s_addc_u32 s27, s42, 0
	v_readfirstlane_b32 s28, v157
	v_lshl_add_u64 v[18:19], s[26:27], 0, v[130:131]
	s_mov_b32 m0, s28
	ds_read_b128 v[106:109], v147 offset:16384
	ds_read_b128 v[110:113], v147 offset:17408
	ds_read_b128 v[122:125], v148 offset:16384
	ds_read_b128 v[126:129], v148 offset:17408
	ds_read_b128 v[160:163], v149 offset:16384
	ds_read_b128 v[164:167], v149 offset:17408
	ds_read_b128 v[168:171], v150 offset:16384
	ds_read_b128 v[172:175], v150 offset:17408
	global_load_lds_dwordx4 v[18:19], off
	v_lshl_add_u64 v[18:19], s[26:27], 0, v[132:133]
	v_readfirstlane_b32 s26, v158
	s_mov_b32 m0, s26
	s_add_u32 s26, s39, 0x100
	global_load_lds_dwordx4 v[18:19], off
	s_addc_u32 s27, s40, 0
	v_readfirstlane_b32 s28, v138
	s_waitcnt vmcnt(4)
	v_lshl_add_u64 v[18:19], s[26:27], 0, v[130:131]
	s_mov_b32 m0, s28
	s_waitcnt lgkmcnt(8)
	s_barrier
	global_load_lds_dwordx4 v[18:19], off
	v_lshl_add_u64 v[18:19], s[26:27], 0, v[132:133]
	v_readfirstlane_b32 s26, v139
	s_mov_b32 m0, s26
	s_nop 0
	global_load_lds_dwordx4 v[18:19], off
	s_waitcnt lgkmcnt(0)
	s_waitcnt lgkmcnt(0)
	v_mfma_f32_16x16x32_f16 v[18:21], v[2:5], v[106:109], v[62:65]
	v_mfma_f32_16x16x32_f16 v[26:29], v[2:5], v[122:125], v[58:61]
	v_mfma_f32_16x16x32_f16 v[34:37], v[2:5], v[160:163], v[114:117]
	v_mfma_f32_16x16x32_f16 v[2:5], v[2:5], v[168:171], v[66:69]
	v_mfma_f32_16x16x32_f16 v[22:25], v[10:13], v[106:109], v[54:57]
	v_mfma_f32_16x16x32_f16 v[30:33], v[10:13], v[122:125], v[50:53]
	v_mfma_f32_16x16x32_f16 v[38:41], v[10:13], v[160:163], v[118:121]
	v_mfma_f32_16x16x32_f16 v[42:45], v[6:9], v[172:175], v[2:5]
	v_mfma_f32_16x16x32_f16 v[2:5], v[10:13], v[168:171], v[70:73]
	v_mfma_f32_16x16x32_f16 v[18:21], v[6:9], v[110:113], v[18:21]
	v_mfma_f32_16x16x32_f16 v[22:25], v[14:17], v[110:113], v[22:25]
	v_mfma_f32_16x16x32_f16 v[26:29], v[6:9], v[126:129], v[26:29]
	v_mfma_f32_16x16x32_f16 v[30:33], v[14:17], v[126:129], v[30:33]
	v_mfma_f32_16x16x32_f16 v[34:37], v[6:9], v[164:167], v[34:37]
	v_mfma_f32_16x16x32_f16 v[38:41], v[14:17], v[164:167], v[38:41]
	v_mfma_f32_16x16x32_f16 v[46:49], v[14:17], v[172:175], v[2:5]
	s_barrier
	s_add_u32 s26, s37, 0x180
	s_addc_u32 s27, s38, 0
	v_readfirstlane_b32 s28, v143
	v_lshl_add_u64 v[2:3], s[26:27], 0, v[130:131]
	s_mov_b32 m0, s28
	ds_read_b128 v[58:61], v159
	ds_read_b128 v[62:65], v159 offset:1024
	ds_read_b128 v[66:69], v159 offset:2048
	ds_read_b128 v[70:73], v159 offset:3072
	global_load_lds_dwordx4 v[2:3], off
	v_lshl_add_u64 v[2:3], s[26:27], 0, v[132:133]
	v_readfirstlane_b32 s26, v144
	s_mov_b32 m0, s26
	s_nop 0
	global_load_lds_dwordx4 v[2:3], off
	s_waitcnt vmcnt(6)
	s_barrier
	s_waitcnt lgkmcnt(0)
	s_waitcnt lgkmcnt(0)
	v_mfma_f32_16x16x32_f16 v[2:5], v[58:61], v[106:109], v[74:77]
	v_mfma_f32_16x16x32_f16 v[10:13], v[58:61], v[122:125], v[82:85]
	v_mfma_f32_16x16x32_f16 v[50:53], v[58:61], v[160:163], v[90:93]
	v_mfma_f32_16x16x32_f16 v[58:61], v[58:61], v[168:171], v[98:101]
	v_mfma_f32_16x16x32_f16 v[2:5], v[62:65], v[110:113], v[2:5]
	v_mfma_f32_16x16x32_f16 v[6:9], v[66:69], v[106:109], v[78:81]
	v_mfma_f32_16x16x32_f16 v[10:13], v[62:65], v[126:129], v[10:13]
	v_mfma_f32_16x16x32_f16 v[14:17], v[66:69], v[122:125], v[86:89]
	v_mfma_f32_16x16x32_f16 v[50:53], v[62:65], v[164:167], v[50:53]
	v_mfma_f32_16x16x32_f16 v[54:57], v[66:69], v[160:163], v[94:97]
	v_mfma_f32_16x16x32_f16 v[58:61], v[62:65], v[172:175], v[58:61]
	v_mfma_f32_16x16x32_f16 v[62:65], v[66:69], v[168:171], v[102:105]
	v_mfma_f32_16x16x32_f16 v[6:9], v[70:73], v[110:113], v[6:9]
	v_mfma_f32_16x16x32_f16 v[14:17], v[70:73], v[126:129], v[14:17]
	v_mfma_f32_16x16x32_f16 v[54:57], v[70:73], v[164:167], v[54:57]
	v_mfma_f32_16x16x32_f16 v[62:65], v[70:73], v[172:175], v[62:65]
	s_barrier
	ds_read_b128 v[98:101], v146
	ds_read_b128 v[102:105], v146 offset:1024
	ds_read_b128 v[106:109], v146 offset:2048
	ds_read_b128 v[110:113], v146 offset:3072
	ds_read_b128 v[90:93], v147 offset:32768
	ds_read_b128 v[94:97], v147 offset:33792
	ds_read_b128 v[66:69], v148 offset:32768
	ds_read_b128 v[86:89], v148 offset:33792
	ds_read_b128 v[70:73], v149 offset:32768
	ds_read_b128 v[74:77], v149 offset:33792
	ds_read_b128 v[78:81], v150 offset:32768
	ds_read_b128 v[82:85], v150 offset:33792
	s_cmp_lt_u32 s17, 60
	s_cselect_b64 s[28:29], -1, 0
	s_cmp_gt_u32 s17, 59
	s_cselect_b64 s[26:27], -1, 0
	s_mov_b64 s[30:31], -1
	s_and_b64 vcc, exec, s[26:27]
	s_cbranch_vccz .LBB2_13
	s_waitcnt vmcnt(0)
	s_mov_b64 s[30:31], 0

.LBB2_15:
	s_add_u32 s30, s39, 0x180
	s_addc_u32 s31, s40, 0
	v_readfirstlane_b32 s34, v153
	v_lshl_add_u64 v[114:115], s[30:31], 0, v[130:131]
	s_mov_b32 m0, s34
	s_waitcnt lgkmcnt(8)
	s_barrier
	global_load_lds_dwordx4 v[114:115], off
	v_lshl_add_u64 v[114:115], s[30:31], 0, v[132:133]
	v_readfirstlane_b32 s30, v154
	s_mov_b32 m0, s30
	s_nop 0
	global_load_lds_dwordx4 v[114:115], off
	s_waitcnt lgkmcnt(0)
	s_waitcnt lgkmcnt(0)
	v_mfma_f32_16x16x32_f16 v[18:21], v[98:101], v[90:93], v[18:21]
	v_mfma_f32_16x16x32_f16 v[22:25], v[106:109], v[90:93], v[22:25]
	v_mfma_f32_16x16x32_f16 v[26:29], v[98:101], v[66:69], v[26:29]
	v_mfma_f32_16x16x32_f16 v[30:33], v[106:109], v[66:69], v[30:33]
	v_mfma_f32_16x16x32_f16 v[34:37], v[98:101], v[70:73], v[34:37]
	v_mfma_f32_16x16x32_f16 v[38:41], v[106:109], v[70:73], v[38:41]
	v_mfma_f32_16x16x32_f16 v[42:45], v[98:101], v[78:81], v[42:45]
	v_mfma_f32_16x16x32_f16 v[46:49], v[106:109], v[78:81], v[46:49]
	v_mfma_f32_16x16x32_f16 v[18:21], v[102:105], v[94:97], v[18:21]
	v_mfma_f32_16x16x32_f16 v[22:25], v[110:113], v[94:97], v[22:25]
	v_mfma_f32_16x16x32_f16 v[26:29], v[102:105], v[86:89], v[26:29]
	v_mfma_f32_16x16x32_f16 v[30:33], v[110:113], v[86:89], v[30:33]
	v_mfma_f32_16x16x32_f16 v[34:37], v[102:105], v[74:77], v[34:37]
	v_mfma_f32_16x16x32_f16 v[38:41], v[110:113], v[74:77], v[38:41]
	v_mfma_f32_16x16x32_f16 v[42:45], v[102:105], v[82:85], v[42:45]
	v_mfma_f32_16x16x32_f16 v[46:49], v[110:113], v[82:85], v[46:49]
	s_barrier
	ds_read_b128 v[98:101], v155
	ds_read_b128 v[102:105], v155 offset:1024
	ds_read_b128 v[106:109], v155 offset:2048
	ds_read_b128 v[110:113], v155 offset:3072
	s_mov_b64 s[30:31], -1
	s_and_b64 vcc, exec, s[26:27]
	s_cbranch_vccz .LBB2_17
	s_waitcnt vmcnt(0)
	s_mov_b64 s[30:31], 0

.LBB2_19:
	s_barrier
	s_waitcnt lgkmcnt(0)
	s_waitcnt lgkmcnt(0)
	v_mfma_f32_16x16x32_f16 v[50:53], v[98:101], v[70:73], v[50:53]
	v_mfma_f32_16x16x32_f16 v[10:13], v[98:101], v[66:69], v[10:13]
	v_mfma_f32_16x16x32_f16 v[14:17], v[106:109], v[66:69], v[14:17]
	v_mfma_f32_16x16x32_f16 v[66:69], v[102:105], v[74:77], v[50:53]
	v_mfma_f32_16x16x32_f16 v[50:53], v[106:109], v[70:73], v[54:57]
	v_mfma_f32_16x16x32_f16 v[70:73], v[110:113], v[74:77], v[50:53]
	v_mfma_f32_16x16x32_f16 v[50:53], v[98:101], v[78:81], v[58:61]
	v_mfma_f32_16x16x32_f16 v[2:5], v[98:101], v[90:93], v[2:5]
	v_mfma_f32_16x16x32_f16 v[6:9], v[106:109], v[90:93], v[6:9]
	v_mfma_f32_16x16x32_f16 v[74:77], v[102:105], v[82:85], v[50:53]
	v_mfma_f32_16x16x32_f16 v[50:53], v[106:109], v[78:81], v[62:65]
	v_mfma_f32_16x16x32_f16 v[2:5], v[102:105], v[94:97], v[2:5]
	v_mfma_f32_16x16x32_f16 v[6:9], v[110:113], v[94:97], v[6:9]
	v_mfma_f32_16x16x32_f16 v[10:13], v[102:105], v[86:89], v[10:13]
	v_mfma_f32_16x16x32_f16 v[14:17], v[110:113], v[86:89], v[14:17]
	v_mfma_f32_16x16x32_f16 v[78:81], v[110:113], v[82:85], v[50:53]
	s_barrier
	ds_read_b128 v[114:117], v156
	ds_read_b128 v[118:121], v156 offset:1024
	ds_read_b128 v[122:125], v156 offset:2048
	ds_read_b128 v[126:129], v156 offset:3072
	ds_read_b128 v[106:109], v147 offset:49152
	ds_read_b128 v[110:113], v147 offset:50176
	ds_read_b128 v[98:101], v148 offset:49152
	ds_read_b128 v[102:105], v148 offset:50176
	ds_read_b128 v[90:93], v149 offset:49152
	ds_read_b128 v[94:97], v149 offset:50176
	ds_read_b128 v[82:85], v150 offset:49152
	ds_read_b128 v[86:89], v150 offset:50176
	s_cmp_gt_u32 s17, 58
	s_cselect_b64 s[30:31], -1, 0
	s_mov_b64 s[34:35], -1
	s_and_b64 vcc, exec, s[30:31]
	s_cbranch_vccz .LBB2_21
	s_waitcnt vmcnt(0)
	s_mov_b64 s[34:35], 0

.LBB2_25:
	s_waitcnt lgkmcnt(0)
	s_waitcnt lgkmcnt(0)
	v_mfma_f32_16x16x32_f16 v[18:21], v[114:117], v[106:109], v[18:21]
	v_mfma_f32_16x16x32_f16 v[62:65], v[118:121], v[110:113], v[18:21]
	v_mfma_f32_16x16x32_f16 v[18:21], v[122:125], v[106:109], v[22:25]
	v_mfma_f32_16x16x32_f16 v[54:57], v[126:129], v[110:113], v[18:21]
	v_mfma_f32_16x16x32_f16 v[18:21], v[114:117], v[98:101], v[26:29]
	v_mfma_f32_16x16x32_f16 v[58:61], v[118:121], v[102:105], v[18:21]
	v_mfma_f32_16x16x32_f16 v[18:21], v[122:125], v[98:101], v[30:33]
	v_mfma_f32_16x16x32_f16 v[50:53], v[126:129], v[102:105], v[18:21]
	v_mfma_f32_16x16x32_f16 v[18:21], v[114:117], v[90:93], v[34:37]
	v_mfma_f32_16x16x32_f16 v[30:33], v[118:121], v[94:97], v[18:21]
	v_mfma_f32_16x16x32_f16 v[18:21], v[122:125], v[90:93], v[38:41]
	v_mfma_f32_16x16x32_f16 v[22:25], v[126:129], v[94:97], v[18:21]
	v_mfma_f32_16x16x32_f16 v[18:21], v[114:117], v[82:85], v[42:45]
	v_mfma_f32_16x16x32_f16 v[26:29], v[118:121], v[86:89], v[18:21]
	v_mfma_f32_16x16x32_f16 v[18:21], v[122:125], v[82:85], v[46:49]
	v_mfma_f32_16x16x32_f16 v[18:21], v[126:129], v[86:89], v[18:21]
	s_barrier
	ds_read_b128 v[114:117], v159
	ds_read_b128 v[118:121], v159 offset:1024
	ds_read_b128 v[122:125], v159 offset:2048
	ds_read_b128 v[126:129], v159 offset:3072
	s_mov_b64 s[28:29], -1
	s_and_b64 vcc, exec, s[30:31]
	s_cbranch_vccz .LBB2_27
	s_waitcnt vmcnt(0)
	s_mov_b64 s[28:29], 0

.LBB2_59:
	ds_read_b128 v[160:163], v157
	ds_read_b128 v[164:167], v157 offset:1024
	ds_read_b128 v[168:171], v157 offset:2048
	ds_read_b128 v[172:175], v157 offset:3072
	s_add_u32 s24, s4, s2
	s_addc_u32 s25, s5, s3
	s_add_u32 s24, s24, 0x80
	s_addc_u32 s25, s25, 0
	v_readfirstlane_b32 s26, v158
	v_lshl_add_u64 v[176:177], s[24:25], 0, v[132:133]
	s_mov_b32 m0, s26
	s_nop 0
	global_load_lds_dwordx4 v[176:177], off
	v_lshl_add_u64 v[176:177], s[24:25], 0, v[130:131]
	v_readfirstlane_b32 s24, v159
	s_mov_b32 m0, s24
	s_nop 0
	global_load_lds_dwordx4 v[176:177], off
	ds_read_b128 v[176:179], v138
	ds_read_b128 v[180:183], v138 offset:1024
	ds_read_b128 v[184:187], v137
	ds_read_b128 v[188:191], v137 offset:1024
	ds_read_b128 v[192:195], v136
	ds_read_b128 v[196:199], v136 offset:1024
	ds_read_b128 v[200:203], v135
	ds_read_b128 v[204:207], v135 offset:1024
	s_waitcnt lgkmcnt(8)
	s_barrier
	s_waitcnt lgkmcnt(0)
	s_waitcnt lgkmcnt(0)
	v_mfma_f32_16x16x32_f16 v[126:129], v[160:163], v[176:179], v[126:129]
	v_mfma_f32_16x16x32_f16 v[122:125], v[168:171], v[176:179], v[122:125]
	v_mfma_f32_16x16x32_f16 v[118:121], v[160:163], v[184:187], v[118:121]
	v_mfma_f32_16x16x32_f16 v[114:117], v[168:171], v[184:187], v[114:117]
	v_mfma_f32_16x16x32_f16 v[110:113], v[160:163], v[192:195], v[110:113]
	v_mfma_f32_16x16x32_f16 v[106:109], v[168:171], v[192:195], v[106:109]
	v_mfma_f32_16x16x32_f16 v[102:105], v[160:163], v[200:203], v[102:105]
	v_mfma_f32_16x16x32_f16 v[98:101], v[168:171], v[200:203], v[98:101]
	v_mfma_f32_16x16x32_f16 v[126:129], v[164:167], v[180:183], v[126:129]
	v_mfma_f32_16x16x32_f16 v[122:125], v[172:175], v[180:183], v[122:125]
	v_mfma_f32_16x16x32_f16 v[118:121], v[164:167], v[188:191], v[118:121]
	v_mfma_f32_16x16x32_f16 v[114:117], v[172:175], v[188:191], v[114:117]
	v_mfma_f32_16x16x32_f16 v[110:113], v[164:167], v[196:199], v[110:113]
	v_mfma_f32_16x16x32_f16 v[106:109], v[172:175], v[196:199], v[106:109]
	v_mfma_f32_16x16x32_f16 v[102:105], v[164:167], v[204:207], v[102:105]
	v_mfma_f32_16x16x32_f16 v[98:101], v[172:175], v[204:207], v[98:101]
	s_barrier
	s_add_u32 s26, s0, s2
	s_addc_u32 s27, s1, s3
	s_add_u32 s24, s26, 0x100
	s_addc_u32 s25, s27, 0
	v_readfirstlane_b32 s28, v141
	v_lshl_add_u64 v[224:225], s[24:25], 0, v[132:133]
	s_mov_b32 m0, s28
	ds_read_b128 v[208:211], v153
	ds_read_b128 v[212:215], v153 offset:1024
	ds_read_b128 v[216:219], v153 offset:2048
	ds_read_b128 v[220:223], v153 offset:3072
	global_load_lds_dwordx4 v[224:225], off
	v_lshl_add_u64 v[224:225], s[24:25], 0, v[130:131]
	v_readfirstlane_b32 s24, v142
	s_mov_b32 m0, s24
	s_nop 0
	global_load_lds_dwordx4 v[224:225], off
	s_barrier
	s_waitcnt lgkmcnt(0)
	s_waitcnt lgkmcnt(0)
	v_mfma_f32_16x16x32_f16 v[94:97], v[208:211], v[176:179], v[94:97]
	v_mfma_f32_16x16x32_f16 v[90:93], v[216:219], v[176:179], v[90:93]
	v_mfma_f32_16x16x32_f16 v[86:89], v[208:211], v[184:187], v[86:89]
	v_mfma_f32_16x16x32_f16 v[82:85], v[216:219], v[184:187], v[82:85]
	v_mfma_f32_16x16x32_f16 v[78:81], v[208:211], v[192:195], v[78:81]
	v_mfma_f32_16x16x32_f16 v[74:77], v[216:219], v[192:195], v[74:77]
	v_mfma_f32_16x16x32_f16 v[70:73], v[208:211], v[200:203], v[70:73]
	v_mfma_f32_16x16x32_f16 v[66:69], v[216:219], v[200:203], v[66:69]
	v_mfma_f32_16x16x32_f16 v[94:97], v[212:215], v[180:183], v[94:97]
	v_mfma_f32_16x16x32_f16 v[90:93], v[220:223], v[180:183], v[90:93]
	v_mfma_f32_16x16x32_f16 v[86:89], v[212:215], v[188:191], v[86:89]
	v_mfma_f32_16x16x32_f16 v[82:85], v[220:223], v[188:191], v[82:85]
	v_mfma_f32_16x16x32_f16 v[78:81], v[212:215], v[196:199], v[78:81]
	v_mfma_f32_16x16x32_f16 v[74:77], v[220:223], v[196:199], v[74:77]
	v_mfma_f32_16x16x32_f16 v[70:73], v[212:215], v[204:207], v[70:73]
	v_mfma_f32_16x16x32_f16 v[66:69], v[220:223], v[204:207], v[66:69]
	s_add_u32 s28, s6, s2
	s_addc_u32 s29, s7, s3
	s_add_u32 s24, s28, 0x100
	s_addc_u32 s25, s29, 0
	v_readfirstlane_b32 s30, v140
	v_lshl_add_u64 v[224:225], s[24:25], 0, v[132:133]
	s_mov_b32 m0, s30
	s_barrier
	ds_read_b128 v[176:179], v138 offset:16384
	ds_read_b128 v[180:183], v138 offset:17408
	ds_read_b128 v[184:187], v137 offset:16384
	ds_read_b128 v[188:191], v137 offset:17408
	ds_read_b128 v[192:195], v136 offset:16384
	ds_read_b128 v[196:199], v136 offset:17408
	ds_read_b128 v[200:203], v135 offset:16384
	ds_read_b128 v[204:207], v135 offset:17408
	global_load_lds_dwordx4 v[224:225], off
	v_lshl_add_u64 v[224:225], s[24:25], 0, v[130:131]
	v_readfirstlane_b32 s24, v144
	s_mov_b32 m0, s24
	s_nop 0
	global_load_lds_dwordx4 v[224:225], off
	s_barrier
	s_waitcnt lgkmcnt(0)
	s_waitcnt lgkmcnt(0)
	v_mfma_f32_16x16x32_f16 v[62:65], v[160:163], v[176:179], v[62:65]
	v_mfma_f32_16x16x32_f16 v[58:61], v[168:171], v[176:179], v[58:61]
	v_mfma_f32_16x16x32_f16 v[54:57], v[160:163], v[184:187], v[54:57]
	v_mfma_f32_16x16x32_f16 v[50:53], v[168:171], v[184:187], v[50:53]
	v_mfma_f32_16x16x32_f16 v[46:49], v[160:163], v[192:195], v[46:49]
	v_mfma_f32_16x16x32_f16 v[42:45], v[168:171], v[192:195], v[42:45]
	v_mfma_f32_16x16x32_f16 v[38:41], v[160:163], v[200:203], v[38:41]
	v_mfma_f32_16x16x32_f16 v[34:37], v[168:171], v[200:203], v[34:37]
	v_mfma_f32_16x16x32_f16 v[62:65], v[164:167], v[180:183], v[62:65]
	v_mfma_f32_16x16x32_f16 v[58:61], v[172:175], v[180:183], v[58:61]
	v_mfma_f32_16x16x32_f16 v[54:57], v[164:167], v[188:191], v[54:57]
	v_mfma_f32_16x16x32_f16 v[50:53], v[172:175], v[188:191], v[50:53]
	v_mfma_f32_16x16x32_f16 v[46:49], v[164:167], v[196:199], v[46:49]
	v_mfma_f32_16x16x32_f16 v[42:45], v[172:175], v[196:199], v[42:45]
	v_mfma_f32_16x16x32_f16 v[38:41], v[164:167], v[204:207], v[38:41]
	v_mfma_f32_16x16x32_f16 v[34:37], v[172:175], v[204:207], v[34:37]
	s_barrier
	s_add_u32 s30, s16, s2
	s_addc_u32 s31, s17, s3
	s_add_u32 s24, s30, 0x100
	s_addc_u32 s25, s31, 0
	v_readfirstlane_b32 s33, v145
	v_lshl_add_u64 v[160:161], s[24:25], 0, v[132:133]
	s_mov_b32 m0, s33
	s_nop 0
	global_load_lds_dwordx4 v[160:161], off
	v_lshl_add_u64 v[160:161], s[24:25], 0, v[130:131]
	v_readfirstlane_b32 s24, v146
	s_mov_b32 m0, s24
	s_nop 0
	global_load_lds_dwordx4 v[160:161], off
	s_mov_b32 s49, s48
	s_add_i32 s48, s48, 1
	s_cmp_gt_u32 s49, 26
	s_cbranch_scc1 .Ls1_plain
	s_cmp_eq_u32 s49, 0
	s_cbranch_scc1 .Ls1_a0
	s_cmp_lt_u32 s49, 8
	s_cbranch_scc1 .Ls1_am
	s_cmp_eq_u32 s49, 8
	s_cbranch_scc1 .Ls1_al
	s_cmp_eq_u32 s49, 9
	s_cbranch_scc1 .Ls1_b0
	s_cmp_lt_u32 s49, 17
	s_cbranch_scc1 .Ls1_bm
	s_cmp_eq_u32 s49, 17
	s_cbranch_scc1 .Ls1_bl
	s_cmp_eq_u32 s49, 18
	s_cbranch_scc1 .Ls1_k0
	s_cmp_lt_u32 s49, 26
	s_cbranch_scc1 .Ls1_km
	s_cmp_eq_u32 s49, 26
	s_cbranch_scc1 .Ls1_kl

.Ls1_join:
	s_barrier
	v_mfma_f32_16x16x32_f16 v[30:33], v[208:211], v[176:179], v[30:33]
	v_mfma_f32_16x16x32_f16 v[26:29], v[216:219], v[176:179], v[26:29]
	v_mfma_f32_16x16x32_f16 v[22:25], v[208:211], v[184:187], v[22:25]
	v_mfma_f32_16x16x32_f16 v[18:21], v[216:219], v[184:187], v[18:21]
	v_mfma_f32_16x16x32_f16 v[14:17], v[208:211], v[192:195], v[14:17]
	v_mfma_f32_16x16x32_f16 v[10:13], v[216:219], v[192:195], v[10:13]
	v_mfma_f32_16x16x32_f16 v[6:9], v[208:211], v[200:203], v[6:9]
	v_mfma_f32_16x16x32_f16 v[2:5], v[216:219], v[200:203], v[2:5]
	v_mfma_f32_16x16x32_f16 v[30:33], v[212:215], v[180:183], v[30:33]
	v_mfma_f32_16x16x32_f16 v[26:29], v[220:223], v[180:183], v[26:29]
	v_mfma_f32_16x16x32_f16 v[22:25], v[212:215], v[188:191], v[22:25]
	v_mfma_f32_16x16x32_f16 v[18:21], v[220:223], v[188:191], v[18:21]
	v_mfma_f32_16x16x32_f16 v[14:17], v[212:215], v[196:199], v[14:17]
	v_mfma_f32_16x16x32_f16 v[10:13], v[220:223], v[196:199], v[10:13]
	v_mfma_f32_16x16x32_f16 v[6:9], v[212:215], v[204:207], v[6:9]
	v_mfma_f32_16x16x32_f16 v[2:5], v[220:223], v[204:207], v[2:5]
	s_barrier
	ds_read_b128 v[160:163], v143
	ds_read_b128 v[164:167], v143 offset:1024
	ds_read_b128 v[168:171], v143 offset:2048
	ds_read_b128 v[172:175], v143 offset:3072
	s_add_u32 s24, s18, s2
	s_addc_u32 s25, s19, s3
	v_readfirstlane_b32 s33, v148
	v_lshl_add_u64 v[208:209], s[24:25], 0, v[132:133]
	s_mov_b32 m0, s33
	ds_read_b128 v[176:179], v138 offset:32768
	ds_read_b128 v[180:183], v138 offset:33792
	ds_read_b128 v[184:187], v137 offset:32768
	ds_read_b128 v[188:191], v137 offset:33792
	ds_read_b128 v[192:195], v136 offset:32768
	ds_read_b128 v[196:199], v136 offset:33792
	ds_read_b128 v[200:203], v135 offset:32768
	ds_read_b128 v[204:207], v135 offset:33792
	global_load_lds_dwordx4 v[208:209], off
	v_lshl_add_u64 v[208:209], s[24:25], 0, v[130:131]
	v_readfirstlane_b32 s24, v149
	s_mov_b32 m0, s24
	s_nop 0
	global_load_lds_dwordx4 v[208:209], off
	s_waitcnt lgkmcnt(8)
	s_barrier
	s_waitcnt lgkmcnt(0)
	s_waitcnt lgkmcnt(0)
	v_mfma_f32_16x16x32_f16 v[126:129], v[160:163], v[176:179], v[126:129]
	v_mfma_f32_16x16x32_f16 v[122:125], v[168:171], v[176:179], v[122:125]
	v_mfma_f32_16x16x32_f16 v[118:121], v[160:163], v[184:187], v[118:121]
	v_mfma_f32_16x16x32_f16 v[114:117], v[168:171], v[184:187], v[114:117]
	v_mfma_f32_16x16x32_f16 v[110:113], v[160:163], v[192:195], v[110:113]
	v_mfma_f32_16x16x32_f16 v[106:109], v[168:171], v[192:195], v[106:109]
	v_mfma_f32_16x16x32_f16 v[102:105], v[160:163], v[200:203], v[102:105]
	v_mfma_f32_16x16x32_f16 v[98:101], v[168:171], v[200:203], v[98:101]
	v_mfma_f32_16x16x32_f16 v[126:129], v[164:167], v[180:183], v[126:129]
	v_mfma_f32_16x16x32_f16 v[122:125], v[172:175], v[180:183], v[122:125]
	v_mfma_f32_16x16x32_f16 v[118:121], v[164:167], v[188:191], v[118:121]
	v_mfma_f32_16x16x32_f16 v[114:117], v[172:175], v[188:191], v[114:117]
	v_mfma_f32_16x16x32_f16 v[110:113], v[164:167], v[196:199], v[110:113]
	v_mfma_f32_16x16x32_f16 v[106:109], v[172:175], v[196:199], v[106:109]
	v_mfma_f32_16x16x32_f16 v[102:105], v[164:167], v[204:207], v[102:105]
	v_mfma_f32_16x16x32_f16 v[98:101], v[172:175], v[204:207], v[98:101]
	s_barrier
	s_add_u32 s24, s26, 0x180
	s_addc_u32 s25, s27, 0
	v_readfirstlane_b32 s26, v150
	v_lshl_add_u64 v[224:225], s[24:25], 0, v[132:133]
	s_mov_b32 m0, s26
	ds_read_b128 v[208:211], v139
	ds_read_b128 v[212:215], v139 offset:1024
	ds_read_b128 v[216:219], v139 offset:2048
	ds_read_b128 v[220:223], v139 offset:3072
	global_load_lds_dwordx4 v[224:225], off
	v_lshl_add_u64 v[224:225], s[24:25], 0, v[130:131]
	v_readfirstlane_b32 s24, v151
	s_mov_b32 m0, s24
	s_nop 0
	global_load_lds_dwordx4 v[224:225], off
	s_barrier
	s_waitcnt lgkmcnt(0)
	s_waitcnt lgkmcnt(0)
	v_mfma_f32_16x16x32_f16 v[94:97], v[208:211], v[176:179], v[94:97]
	v_mfma_f32_16x16x32_f16 v[90:93], v[216:219], v[176:179], v[90:93]
	v_mfma_f32_16x16x32_f16 v[86:89], v[208:211], v[184:187], v[86:89]
	v_mfma_f32_16x16x32_f16 v[82:85], v[216:219], v[184:187], v[82:85]
	v_mfma_f32_16x16x32_f16 v[78:81], v[208:211], v[192:195], v[78:81]
	v_mfma_f32_16x16x32_f16 v[74:77], v[216:219], v[192:195], v[74:77]
	v_mfma_f32_16x16x32_f16 v[70:73], v[208:211], v[200:203], v[70:73]
	v_mfma_f32_16x16x32_f16 v[66:69], v[216:219], v[200:203], v[66:69]
	v_mfma_f32_16x16x32_f16 v[94:97], v[212:215], v[180:183], v[94:97]
	v_mfma_f32_16x16x32_f16 v[90:93], v[220:223], v[180:183], v[90:93]
	v_mfma_f32_16x16x32_f16 v[86:89], v[212:215], v[188:191], v[86:89]
	v_mfma_f32_16x16x32_f16 v[82:85], v[220:223], v[188:191], v[82:85]
	v_mfma_f32_16x16x32_f16 v[78:81], v[212:215], v[196:199], v[78:81]
	v_mfma_f32_16x16x32_f16 v[74:77], v[220:223], v[196:199], v[74:77]
	v_mfma_f32_16x16x32_f16 v[70:73], v[212:215], v[204:207], v[70:73]
	v_mfma_f32_16x16x32_f16 v[66:69], v[220:223], v[204:207], v[66:69]
	s_add_u32 s24, s28, 0x180
	s_addc_u32 s25, s29, 0
	v_readfirstlane_b32 s26, v152
	v_lshl_add_u64 v[224:225], s[24:25], 0, v[132:133]
	s_mov_b32 m0, s26
	s_barrier
	ds_read_b128 v[176:179], v138 offset:49152
	ds_read_b128 v[180:183], v138 offset:50176
	ds_read_b128 v[184:187], v137 offset:49152
	ds_read_b128 v[188:191], v137 offset:50176
	ds_read_b128 v[192:195], v136 offset:49152
	ds_read_b128 v[196:199], v136 offset:50176
	ds_read_b128 v[200:203], v135 offset:49152
	ds_read_b128 v[204:207], v135 offset:50176
	global_load_lds_dwordx4 v[224:225], off
	v_lshl_add_u64 v[224:225], s[24:25], 0, v[130:131]
	v_readfirstlane_b32 s24, v154
	s_mov_b32 m0, s24
	s_nop 0
	global_load_lds_dwordx4 v[224:225], off
	s_barrier
	s_waitcnt lgkmcnt(0)
	s_waitcnt lgkmcnt(0)
	v_mfma_f32_16x16x32_f16 v[62:65], v[160:163], v[176:179], v[62:65]
	v_mfma_f32_16x16x32_f16 v[58:61], v[168:171], v[176:179], v[58:61]
	v_mfma_f32_16x16x32_f16 v[54:57], v[160:163], v[184:187], v[54:57]
	v_mfma_f32_16x16x32_f16 v[50:53], v[168:171], v[184:187], v[50:53]
	v_mfma_f32_16x16x32_f16 v[46:49], v[160:163], v[192:195], v[46:49]
	v_mfma_f32_16x16x32_f16 v[42:45], v[168:171], v[192:195], v[42:45]
	v_mfma_f32_16x16x32_f16 v[38:41], v[160:163], v[200:203], v[38:41]
	v_mfma_f32_16x16x32_f16 v[34:37], v[168:171], v[200:203], v[34:37]
	v_mfma_f32_16x16x32_f16 v[62:65], v[164:167], v[180:183], v[62:65]
	v_mfma_f32_16x16x32_f16 v[58:61], v[172:175], v[180:183], v[58:61]
	v_mfma_f32_16x16x32_f16 v[54:57], v[164:167], v[188:191], v[54:57]
	v_mfma_f32_16x16x32_f16 v[50:53], v[172:175], v[188:191], v[50:53]
	v_mfma_f32_16x16x32_f16 v[46:49], v[164:167], v[196:199], v[46:49]
	v_mfma_f32_16x16x32_f16 v[42:45], v[172:175], v[196:199], v[42:45]
	v_mfma_f32_16x16x32_f16 v[38:41], v[164:167], v[204:207], v[38:41]
	v_mfma_f32_16x16x32_f16 v[34:37], v[172:175], v[204:207], v[34:37]
	s_barrier
	s_add_u32 s24, s30, 0x180
	s_addc_u32 s25, s31, 0
	v_readfirstlane_b32 s26, v155
	v_lshl_add_u64 v[160:161], s[24:25], 0, v[132:133]
	s_mov_b32 m0, s26
	s_nop 0
	global_load_lds_dwordx4 v[160:161], off
	v_lshl_add_u64 v[160:161], s[24:25], 0, v[130:131]
	v_readfirstlane_b32 s24, v156
	s_mov_b32 m0, s24
	s_nop 0
	global_load_lds_dwordx4 v[160:161], off
	s_cmp_eq_u32 s49, 9
	s_cbranch_scc1 .Ls2_arr2
	s_cmp_eq_u32 s49, 12
	s_cbranch_scc1 .Ls2_poll2
	s_cmp_eq_u32 s49, 18
	s_cbranch_scc1 .Ls2_arr3
	s_cmp_eq_u32 s49, 21
	s_cbranch_scc1 .Ls2_poll3

.Ls2_join:
	s_barrier
	v_mfma_f32_16x16x32_f16 v[30:33], v[208:211], v[176:179], v[30:33]
	v_mfma_f32_16x16x32_f16 v[26:29], v[216:219], v[176:179], v[26:29]
	v_mfma_f32_16x16x32_f16 v[22:25], v[208:211], v[184:187], v[22:25]
	v_mfma_f32_16x16x32_f16 v[18:21], v[216:219], v[184:187], v[18:21]
	v_mfma_f32_16x16x32_f16 v[14:17], v[208:211], v[192:195], v[14:17]
	v_mfma_f32_16x16x32_f16 v[10:13], v[216:219], v[192:195], v[10:13]
	v_mfma_f32_16x16x32_f16 v[6:9], v[208:211], v[200:203], v[6:9]
	v_mfma_f32_16x16x32_f16 v[2:5], v[216:219], v[200:203], v[2:5]
	v_mfma_f32_16x16x32_f16 v[30:33], v[212:215], v[180:183], v[30:33]
	v_mfma_f32_16x16x32_f16 v[26:29], v[220:223], v[180:183], v[26:29]
	v_mfma_f32_16x16x32_f16 v[22:25], v[212:215], v[188:191], v[22:25]
	v_mfma_f32_16x16x32_f16 v[18:21], v[220:223], v[188:191], v[18:21]
	v_mfma_f32_16x16x32_f16 v[14:17], v[212:215], v[196:199], v[14:17]
	v_mfma_f32_16x16x32_f16 v[10:13], v[220:223], v[196:199], v[10:13]
	v_mfma_f32_16x16x32_f16 v[6:9], v[212:215], v[204:207], v[6:9]
	v_mfma_f32_16x16x32_f16 v[2:5], v[220:223], v[204:207], v[2:5]
	s_add_i32 s23, s23, 2
	s_add_u32 s2, s2, 0x100
	s_addc_u32 s3, s3, 0
	s_cmp_lt_u32 s23, 60
	s_barrier
	s_cbranch_scc1 .LBB2_59
	s_add_u32 s0, s14, 0x1f80
	v_add_u32_e32 v141, 0xc000, v140
	s_addc_u32 s1, s15, 0
	v_readfirstlane_b32 s2, v141
	v_lshl_add_u64 v[132:133], s[0:1], 0, v[132:133]
	s_mov_b32 m0, s2
	ds_read_b128 v[148:151], v157
	ds_read_b128 v[158:161], v157 offset:1024
	ds_read_b128 v[162:165], v157 offset:2048
	ds_read_b128 v[154:157], v157 offset:3072
	global_load_lds_dwordx4 v[132:133], off
	v_add_u32_e32 v132, 0xe000, v140
	v_lshl_add_u64 v[130:131], s[0:1], 0, v[130:131]
	v_readfirstlane_b32 s0, v132
	s_mov_b32 m0, s0
	s_nop 0
	global_load_lds_dwordx4 v[130:131], off
	ds_read_b128 v[130:133], v138
	ds_read_b128 v[166:169], v138 offset:1024
	ds_read_b128 v[170:173], v137
	ds_read_b128 v[174:177], v137 offset:1024
	ds_read_b128 v[178:181], v136
	ds_read_b128 v[182:185], v136 offset:1024
	ds_read_b128 v[186:189], v135
	ds_read_b128 v[190:193], v135 offset:1024
	s_barrier
	s_waitcnt lgkmcnt(0)
	s_waitcnt lgkmcnt(0)
	v_mfma_f32_16x16x32_f16 v[126:129], v[148:151], v[130:133], v[126:129]
	v_mfma_f32_16x16x32_f16 v[122:125], v[162:165], v[130:133], v[122:125]
	v_mfma_f32_16x16x32_f16 v[118:121], v[148:151], v[170:173], v[118:121]
	v_mfma_f32_16x16x32_f16 v[114:117], v[162:165], v[170:173], v[114:117]
	v_mfma_f32_16x16x32_f16 v[110:113], v[148:151], v[178:181], v[110:113]
	v_mfma_f32_16x16x32_f16 v[106:109], v[162:165], v[178:181], v[106:109]
	v_mfma_f32_16x16x32_f16 v[102:105], v[148:151], v[186:189], v[102:105]
	v_mfma_f32_16x16x32_f16 v[126:129], v[158:161], v[166:169], v[126:129]
	v_mfma_f32_16x16x32_f16 v[122:125], v[154:157], v[166:169], v[122:125]
	v_mfma_f32_16x16x32_f16 v[118:121], v[158:161], v[174:177], v[118:121]
	v_mfma_f32_16x16x32_f16 v[114:117], v[154:157], v[174:177], v[114:117]
	v_mfma_f32_16x16x32_f16 v[110:113], v[158:161], v[182:185], v[110:113]
	v_mfma_f32_16x16x32_f16 v[106:109], v[154:157], v[182:185], v[106:109]
	v_mfma_f32_16x16x32_f16 v[102:105], v[158:161], v[190:193], v[102:105]
	v_mfma_f32_16x16x32_f16 v[98:101], v[162:165], v[186:189], v[98:101]
	v_mfma_f32_16x16x32_f16 v[194:197], v[154:157], v[190:193], v[98:101]
	s_barrier
	s_nop 4
	ds_read_b128 v[98:101], v153
	ds_read_b128 v[198:201], v153 offset:1024
	ds_read_b128 v[202:205], v153 offset:2048
	ds_read_b128 v[206:209], v153 offset:3072
	s_barrier
	s_waitcnt lgkmcnt(0)
	s_waitcnt lgkmcnt(0)
	v_mfma_f32_16x16x32_f16 v[82:85], v[202:205], v[170:173], v[82:85]
	v_mfma_f32_16x16x32_f16 v[78:81], v[98:101], v[178:181], v[78:81]
	v_mfma_f32_16x16x32_f16 v[74:77], v[202:205], v[178:181], v[74:77]
	v_mfma_f32_16x16x32_f16 v[70:73], v[98:101], v[186:189], v[70:73]
	v_mfma_f32_16x16x32_f16 v[94:97], v[98:101], v[130:133], v[94:97]
	v_mfma_f32_16x16x32_f16 v[90:93], v[202:205], v[130:133], v[90:93]
	v_mfma_f32_16x16x32_f16 v[86:89], v[98:101], v[170:173], v[86:89]
	v_mfma_f32_16x16x32_f16 v[82:85], v[206:209], v[174:177], v[82:85]
	v_mfma_f32_16x16x32_f16 v[78:81], v[198:201], v[182:185], v[78:81]
	v_mfma_f32_16x16x32_f16 v[74:77], v[206:209], v[182:185], v[74:77]
	v_mfma_f32_16x16x32_f16 v[70:73], v[198:201], v[190:193], v[70:73]
	v_mfma_f32_16x16x32_f16 v[66:69], v[202:205], v[186:189], v[66:69]
	v_mfma_f32_16x16x32_f16 v[210:213], v[198:201], v[166:169], v[94:97]
	v_mfma_f32_16x16x32_f16 v[166:169], v[206:209], v[166:169], v[90:93]
	v_mfma_f32_16x16x32_f16 v[214:217], v[198:201], v[174:177], v[86:89]
	v_mfma_f32_16x16x32_f16 v[66:69], v[206:209], v[190:193], v[66:69]
	s_barrier
	ds_read_b128 v[86:89], v138 offset:16384
	ds_read_b128 v[90:93], v138 offset:17408
	ds_read_b128 v[94:97], v137 offset:16384
	ds_read_b128 v[130:133], v137 offset:17408
	ds_read_b128 v[170:173], v136 offset:16384
	ds_read_b128 v[174:177], v136 offset:17408
	ds_read_b128 v[178:181], v135 offset:16384
	ds_read_b128 v[182:185], v135 offset:17408
	s_waitcnt vmcnt(4)
	s_barrier
	s_waitcnt lgkmcnt(0)
	s_waitcnt lgkmcnt(0)
	v_mfma_f32_16x16x32_f16 v[62:65], v[148:151], v[86:89], v[62:65]
	v_mfma_f32_16x16x32_f16 v[54:57], v[148:151], v[94:97], v[54:57]
	v_mfma_f32_16x16x32_f16 v[46:49], v[148:151], v[170:173], v[46:49]
	v_mfma_f32_16x16x32_f16 v[42:45], v[162:165], v[170:173], v[42:45]
	v_mfma_f32_16x16x32_f16 v[38:41], v[148:151], v[178:181], v[38:41]
	v_mfma_f32_16x16x32_f16 v[34:37], v[162:165], v[178:181], v[34:37]
	v_mfma_f32_16x16x32_f16 v[62:65], v[158:161], v[90:93], v[62:65]
	v_mfma_f32_16x16x32_f16 v[58:61], v[162:165], v[86:89], v[58:61]
	v_mfma_f32_16x16x32_f16 v[54:57], v[158:161], v[130:133], v[54:57]
	v_mfma_f32_16x16x32_f16 v[50:53], v[162:165], v[94:97], v[50:53]
	v_mfma_f32_16x16x32_f16 v[46:49], v[158:161], v[174:177], v[46:49]
	v_mfma_f32_16x16x32_f16 v[42:45], v[154:157], v[174:177], v[42:45]
	v_mfma_f32_16x16x32_f16 v[38:41], v[158:161], v[182:185], v[38:41]
	v_mfma_f32_16x16x32_f16 v[34:37], v[154:157], v[182:185], v[34:37]
	v_mfma_f32_16x16x32_f16 v[186:189], v[154:157], v[90:93], v[58:61]
	v_mfma_f32_16x16x32_f16 v[190:193], v[154:157], v[130:133], v[50:53]
	v_mfma_f32_16x16x32_f16 v[14:17], v[98:101], v[170:173], v[14:17]
	v_mfma_f32_16x16x32_f16 v[6:9], v[98:101], v[178:181], v[6:9]
	v_mfma_f32_16x16x32_f16 v[30:33], v[98:101], v[86:89], v[30:33]
	v_mfma_f32_16x16x32_f16 v[26:29], v[202:205], v[86:89], v[26:29]
	v_mfma_f32_16x16x32_f16 v[22:25], v[98:101], v[94:97], v[22:25]
	v_mfma_f32_16x16x32_f16 v[18:21], v[202:205], v[94:97], v[18:21]
	v_mfma_f32_16x16x32_f16 v[14:17], v[198:201], v[174:177], v[14:17]
	v_mfma_f32_16x16x32_f16 v[10:13], v[202:205], v[170:173], v[10:13]
	v_mfma_f32_16x16x32_f16 v[6:9], v[198:201], v[182:185], v[6:9]
	v_mfma_f32_16x16x32_f16 v[2:5], v[202:205], v[178:181], v[2:5]
	v_mfma_f32_16x16x32_f16 v[148:151], v[198:201], v[90:93], v[30:33]
	v_mfma_f32_16x16x32_f16 v[152:155], v[206:209], v[90:93], v[26:29]
	v_mfma_f32_16x16x32_f16 v[156:159], v[198:201], v[130:133], v[22:25]
	v_mfma_f32_16x16x32_f16 v[160:163], v[206:209], v[130:133], v[18:21]
	v_mfma_f32_16x16x32_f16 v[170:173], v[206:209], v[174:177], v[10:13]
	v_mfma_f32_16x16x32_f16 v[174:177], v[206:209], v[182:185], v[2:5]
	s_barrier
	s_nop 0
	ds_read_b128 v[2:5], v143
	ds_read_b128 v[10:13], v143 offset:1024
	ds_read_b128 v[22:25], v143 offset:2048
	ds_read_b128 v[140:143], v143 offset:3072
	ds_read_b128 v[18:21], v138 offset:32768
	ds_read_b128 v[26:29], v138 offset:33792
	ds_read_b128 v[30:33], v137 offset:32768
	ds_read_b128 v[50:53], v137 offset:33792
	ds_read_b128 v[58:61], v136 offset:32768
	ds_read_b128 v[178:181], v136 offset:33792
	ds_read_b128 v[182:185], v135 offset:32768
	ds_read_b128 v[198:201], v135 offset:33792
	s_waitcnt vmcnt(2)
	s_barrier
	s_waitcnt lgkmcnt(0)
	s_waitcnt lgkmcnt(0)
	v_mfma_f32_16x16x32_f16 v[86:89], v[2:5], v[18:21], v[126:129]
	v_mfma_f32_16x16x32_f16 v[126:129], v[10:13], v[26:29], v[86:89]
	v_mfma_f32_16x16x32_f16 v[86:89], v[22:25], v[18:21], v[122:125]
	v_mfma_f32_16x16x32_f16 v[130:133], v[140:143], v[26:29], v[86:89]
	v_mfma_f32_16x16x32_f16 v[86:89], v[2:5], v[30:33], v[118:121]
	v_mfma_f32_16x16x32_f16 v[118:121], v[10:13], v[50:53], v[86:89]
	v_mfma_f32_16x16x32_f16 v[86:89], v[22:25], v[30:33], v[114:117]
	v_mfma_f32_16x16x32_f16 v[122:125], v[140:143], v[50:53], v[86:89]
	v_mfma_f32_16x16x32_f16 v[86:89], v[2:5], v[58:61], v[110:113]
	v_mfma_f32_16x16x32_f16 v[94:97], v[10:13], v[178:181], v[86:89]
	v_mfma_f32_16x16x32_f16 v[86:89], v[22:25], v[58:61], v[106:109]
	v_mfma_f32_16x16x32_f16 v[98:101], v[140:143], v[178:181], v[86:89]
	v_mfma_f32_16x16x32_f16 v[86:89], v[2:5], v[182:185], v[102:105]
	v_mfma_f32_16x16x32_f16 v[90:93], v[22:25], v[182:185], v[194:197]
	v_mfma_f32_16x16x32_f16 v[86:89], v[10:13], v[198:201], v[86:89]
	v_mfma_f32_16x16x32_f16 v[90:93], v[140:143], v[198:201], v[90:93]
	s_barrier
	ds_read_b128 v[194:197], v139
	ds_read_b128 v[202:205], v139 offset:1024
	ds_read_b128 v[206:209], v139 offset:2048
	ds_read_b128 v[218:221], v139 offset:3072
	s_waitcnt vmcnt(0)
	s_barrier
	s_and_saveexec_b64 s[52:53], s[56:57]
	s_cbranch_execz .Lkv_noarrive
	v_mov_b32_e32 v228, 0
	v_mov_b32_e32 v229, 1
	global_atomic_add v228, v229, s[54:55] sc1
.Lkv_noarrive:
	s_or_b64 exec, exec, s[52:53]
	s_waitcnt lgkmcnt(0)
	s_waitcnt lgkmcnt(0)
	v_mfma_f32_16x16x32_f16 v[102:105], v[194:197], v[18:21], v[210:213]
	v_mfma_f32_16x16x32_f16 v[18:21], v[206:209], v[18:21], v[166:169]
	v_mfma_f32_16x16x32_f16 v[114:117], v[218:221], v[26:29], v[18:21]
	v_mfma_f32_16x16x32_f16 v[18:21], v[194:197], v[30:33], v[214:217]
	v_mfma_f32_16x16x32_f16 v[110:113], v[202:205], v[26:29], v[102:105]
	v_mfma_f32_16x16x32_f16 v[102:105], v[202:205], v[50:53], v[18:21]
	v_mfma_f32_16x16x32_f16 v[18:21], v[206:209], v[30:33], v[82:85]
	v_mfma_f32_16x16x32_f16 v[106:109], v[218:221], v[50:53], v[18:21]
	v_mfma_f32_16x16x32_f16 v[18:21], v[194:197], v[58:61], v[78:81]
	v_mfma_f32_16x16x32_f16 v[78:81], v[202:205], v[178:181], v[18:21]
	v_mfma_f32_16x16x32_f16 v[18:21], v[206:209], v[58:61], v[74:77]
	v_mfma_f32_16x16x32_f16 v[82:85], v[218:221], v[178:181], v[18:21]
	v_mfma_f32_16x16x32_f16 v[18:21], v[194:197], v[182:185], v[70:73]
	v_mfma_f32_16x16x32_f16 v[70:73], v[202:205], v[198:201], v[18:21]
	v_mfma_f32_16x16x32_f16 v[18:21], v[206:209], v[182:185], v[66:69]
	v_mfma_f32_16x16x32_f16 v[74:77], v[218:221], v[198:201], v[18:21]
	s_barrier
	ds_read_b128 v[66:69], v138 offset:49152
	ds_read_b128 v[164:167], v138 offset:50176
	ds_read_b128 v[178:181], v137 offset:49152
	ds_read_b128 v[182:185], v137 offset:50176
	ds_read_b128 v[198:201], v136 offset:49152
	ds_read_b128 v[136:139], v136 offset:50176
	ds_read_b128 v[210:213], v135 offset:49152
	ds_read_b128 v[214:217], v135 offset:50176
	s_barrier
	s_waitcnt lgkmcnt(0)
	s_waitcnt lgkmcnt(0)
	v_mfma_f32_16x16x32_f16 v[18:21], v[2:5], v[66:69], v[62:65]
	v_mfma_f32_16x16x32_f16 v[58:61], v[10:13], v[164:167], v[18:21]
	v_mfma_f32_16x16x32_f16 v[18:21], v[22:25], v[66:69], v[186:189]
	v_mfma_f32_16x16x32_f16 v[62:65], v[140:143], v[164:167], v[18:21]
	v_mfma_f32_16x16x32_f16 v[18:21], v[2:5], v[178:181], v[54:57]
	v_mfma_f32_16x16x32_f16 v[50:53], v[10:13], v[182:185], v[18:21]
	v_mfma_f32_16x16x32_f16 v[18:21], v[22:25], v[178:181], v[190:193]
	v_mfma_f32_16x16x32_f16 v[54:57], v[140:143], v[182:185], v[18:21]
	v_mfma_f32_16x16x32_f16 v[18:21], v[2:5], v[198:201], v[46:49]
	v_mfma_f32_16x16x32_f16 v[26:29], v[10:13], v[136:139], v[18:21]
	v_mfma_f32_16x16x32_f16 v[18:21], v[22:25], v[198:201], v[42:45]
	v_mfma_f32_16x16x32_f16 v[2:5], v[2:5], v[210:213], v[38:41]
	v_mfma_f32_16x16x32_f16 v[30:33], v[140:143], v[136:139], v[18:21]
	v_mfma_f32_16x16x32_f16 v[18:21], v[10:13], v[214:217], v[2:5]
	v_mfma_f32_16x16x32_f16 v[2:5], v[22:25], v[210:213], v[34:37]
	v_mfma_f32_16x16x32_f16 v[22:25], v[140:143], v[214:217], v[2:5]
	v_mfma_f32_16x16x32_f16 v[2:5], v[194:197], v[66:69], v[148:151]
	v_mfma_f32_16x16x32_f16 v[42:45], v[202:205], v[164:167], v[2:5]
	v_mfma_f32_16x16x32_f16 v[2:5], v[206:209], v[66:69], v[152:155]
	v_mfma_f32_16x16x32_f16 v[46:49], v[218:221], v[164:167], v[2:5]
	v_mfma_f32_16x16x32_f16 v[2:5], v[194:197], v[178:181], v[156:159]
	v_mfma_f32_16x16x32_f16 v[34:37], v[202:205], v[182:185], v[2:5]
	v_mfma_f32_16x16x32_f16 v[2:5], v[206:209], v[178:181], v[160:163]
	v_mfma_f32_16x16x32_f16 v[38:41], v[218:221], v[182:185], v[2:5]
	v_mfma_f32_16x16x32_f16 v[2:5], v[194:197], v[198:201], v[14:17]
	v_mfma_f32_16x16x32_f16 v[10:13], v[202:205], v[136:139], v[2:5]
	v_mfma_f32_16x16x32_f16 v[2:5], v[206:209], v[198:201], v[170:173]
	v_mfma_f32_16x16x32_f16 v[14:17], v[218:221], v[136:139], v[2:5]
	v_mfma_f32_16x16x32_f16 v[2:5], v[194:197], v[210:213], v[6:9]
	v_mfma_f32_16x16x32_f16 v[6:9], v[206:209], v[210:213], v[174:177]
	v_mfma_f32_16x16x32_f16 v[2:5], v[202:205], v[214:217], v[2:5]
	v_mfma_f32_16x16x32_f16 v[6:9], v[218:221], v[214:217], v[6:9]
	s_movk_i32 s0, 0x100
	v_cmp_gt_u32_e32 vcc, s0, v0
	s_barrier
	s_and_saveexec_b64 s[0:1], vcc
	s_cbranch_execz .LBB2_62
	s_barrier
